# read-once loads marked nt (P3 short-conv gate rows, SSD z rows) to keep the next phase's inputs cached, on top of combo5
# speedup vs baseline: 1.0003x; 1.0003x over previous
; #define GAS __attribute__((address_space(1)))
; __device__ __forceinline__ void ssd_unit(LAS unsigned char* lds, int b, int h, const bf16* PROJ, const bf16* CONV, const float* dt_bias, const float* a_log, const float* ssd_d,
;                                          bf16* Y, float* SSQ, int tid, int wave, int lane) {
;     ...
;         u32x2 zv[4];
; #pragma unroll
;         for (int j = 0; j < 4; ++j) zv[j] = *(const GAS u32x2*)(projb + (unsigned)(((rowbase + t0 + 16 * (4 * th + j) + r) * PP + O_Z + h * 64 + 16 * pb + 4 * q) * 2));
.LBB0_381:
	s_add_i32 s0, s6, s90
	v_add_u32_e32 v154, s20, v98
	v_add_u32_e32 v199, s0, v181
	v_mad_u64_u32 v[66:67], s[0:1], v199, s76, v[154:155]
	s_add_i32 s0, s81, s90
	s_nop 0
	v_add_u32_e32 v68, s0, v181
	v_add_u32_e32 v67, 0x92000, v66
	v_add_u32_e32 v70, 0x124000, v66
	v_mad_u64_u32 v[68:69], s[0:1], v68, s76, v[154:155]
	global_load_dwordx2 v[162:163], v66, s[10:11] nt
	global_load_dwordx2 v[160:161], v67, s[10:11] nt
	global_load_dwordx2 v[158:159], v70, s[10:11] nt
	global_load_dwordx2 v[156:157], v68, s[10:11] nt
	v_lshlrev_b32_e32 v66, 3, v117
	s_mul_i32 s89, s89, 0x180000
	s_and_saveexec_b64 s[0:1], s[48:49]
	s_cbranch_execz .LBB0_383
	v_readlane_b32 s48, v248, 25
	v_or_b32_e32 v3, v66, v176
	s_nop 0
	v_lshl_or_b32 v2, v115, 3, s48
	v_cndmask_b32_e64 v2, v3, v2, s[46:47]
	v_add_u32_e32 v3, s80, v116
	v_mad_u64_u32 v[2:3], s[46:47], v3, s4, v[2:3]
	v_lshl_add_u32 v26, v2, 1, s89
	v_add_u32_e32 v6, 0x3000, v26
	v_add_u32_e32 v10, 0x6000, v26
	v_add_u32_e32 v14, 0x9000, v26
	v_add_u32_e32 v18, 0xc000, v26
	v_add_u32_e32 v22, 0xf000, v26
	v_add_u32_e32 v27, 0x12000, v26
	v_add_u32_e32 v30, 0x15000, v26
	global_load_dwordx4 v[2:5], v26, s[8:9]
	s_nop 0
	global_load_dwordx4 v[6:9], v6, s[8:9]
	s_nop 0
	global_load_dwordx4 v[10:13], v10, s[8:9]
	s_nop 0
	global_load_dwordx4 v[14:17], v14, s[8:9]
	s_nop 0
	global_load_dwordx4 v[18:21], v18, s[8:9]
	s_nop 0
	global_load_dwordx4 v[22:25], v22, s[8:9]
	s_nop 0
	global_load_dwordx4 v[26:29], v27, s[8:9]
	s_nop 0
	global_load_dwordx4 v[30:33], v30, s[8:9]

; #define GAS __attribute__((address_space(1)))
; __device__ __forceinline__ void p3_rows2(int row0, const bf16* PROJ, const float* sc_w, const float* sc_nw, const float* ssd_nw, const float* SSQ, bf16* Y, LAS unsigned char* scr, int lane) {
;     ...
; #pragma unroll 2
;     for (int i = 0; i < 8; ++i) {
;         const int c0 = (i * 64 + lane) * 8; const bf16* q = pr + i * 512; const bf16* qh = halo ? q : q + 2 * PP;
;         const u32x4 um2v = *(const GAS u32x4*)(qh - 2 * PP + O_U), um1v = *(const GAS u32x4*)(qh - PP + O_U), u0v = *(const GAS u32x4*)(q + O_U), u1v = *(const GAS u32x4*)(q + PP + O_U);
;         const u32x4 b0v = *(const GAS u32x4*)(q + O_SCB), b1v = *(const GAS u32x4*)(q + PP + O_SCB);
;         const f32x4 w0a = *(const GAS f32x4*)(sc_w + c0), w0b = *(const GAS f32x4*)(sc_w + c0 + 4), w1a = *(const GAS f32x4*)(sc_w + D_CONV + c0), w1b = *(const GAS f32x4*)(sc_w + D_CONV + c0 + 4),
;                     w2a = *(const GAS f32x4*)(sc_w + 2 * D_CONV + c0), w2b = *(const GAS f32x4*)(sc_w + 2 * D_CONV + c0 + 4);
.LBB0_485:
	v_lshl_add_u64 v[26:27], v[6:7], 0, s[2:3]
	s_waitcnt vmcnt(0)
	v_add_co_u32_e32 v76, vcc, 0xfffe3000, v26
	v_lshl_add_u64 v[24:25], v[14:15], 0, s[4:5]
	s_nop 0
	v_addc_co_u32_e32 v77, vcc, -1, v27, vcc
	v_add_co_u32_e32 v26, vcc, 0xfffec000, v26
	global_load_dwordx4 v[2:5], v[6:7], off offset:-1024 nt
	s_nop 0
	v_addc_co_u32_e32 v27, vcc, -1, v27, vcc
	v_add_co_u32_e32 v82, vcc, 0xffff5000, v6
	global_load_dwordx4 v[32:35], v[24:25], off offset:16
	global_load_dwordx4 v[36:39], v[24:25], off
	v_addc_co_u32_e32 v83, vcc, -1, v7, vcc
	v_add_co_u32_e32 v84, vcc, 0xffffe000, v6
	global_load_dwordx4 v[40:43], v[76:77], off offset:-2560
	global_load_dwordx4 v[44:47], v[26:27], off offset:-2048
	v_addc_co_u32_e32 v85, vcc, -1, v7, vcc
	v_add_co_u32_e32 v86, vcc, 0xffff7000, v6
	v_lshl_add_u64 v[64:65], v[24:25], 0, s[18:19]
	s_nop 0
	v_addc_co_u32_e32 v87, vcc, -1, v7, vcc
	v_add_co_u32_e32 v88, vcc, s34, v24
	v_lshl_add_u64 v[72:73], v[24:25], 0, s[20:21]
	s_nop 0
	v_addc_co_u32_e32 v89, vcc, 0, v25, vcc
	v_add_co_u32_e32 v90, vcc, s35, v24
	global_load_dwordx4 v[48:51], v[82:83], off offset:-1536
	global_load_dwordx4 v[52:55], v[84:85], off offset:-1024
	v_addc_co_u32_e32 v91, vcc, 0, v25, vcc
	global_load_dwordx4 v[56:59], v[86:87], off offset:-1536 nt
	global_load_dwordx4 v[60:63], v[88:89], off
	s_nop 0
	global_load_dwordx4 v[64:67], v[64:65], off offset:16
	s_nop 0
	global_load_dwordx4 v[68:71], v[90:91], off
	s_nop 0
	global_load_dwordx4 v[72:75], v[72:73], off offset:16
	v_lshl_add_u64 v[78:79], v[24:25], 0, s[22:23]
	v_lshl_add_u64 v[80:81], v[24:25], 0, s[24:25]
	global_load_dwordx4 v[184:187], v[76:77], off offset:-1536
	global_load_dwordx4 v[188:191], v[26:27], off offset:-1024
	global_load_dwordx4 v[192:195], v[82:83], off offset:-512
	global_load_dwordx4 v[196:199], v[84:85], off
	global_load_dwordx4 v[200:203], v[86:87], off offset:-512 nt
	global_load_dwordx4 v[204:207], v[6:7], off nt
	global_load_dwordx4 v[208:211], v[90:91], off offset:2048
	global_load_dwordx4 v[212:215], v[24:25], off offset:2048
	global_load_dwordx4 v[216:219], v[88:89], off offset:2048
	global_load_dwordx4 v[220:223], v[80:81], off offset:16
	global_load_dwordx4 v[140:143], v[24:25], off offset:2064
	global_load_dwordx4 v[224:227], v[78:79], off offset:16
	s_add_u32 s4, s4, 0x1000
	s_addc_u32 s5, s5, 0
	s_cmpk_eq_i32 s4, 0x4000
	s_waitcnt vmcnt(23)
	v_lshlrev_b32_e32 v93, 16, v2
	v_and_b32_e32 v95, 0xffff0000, v2
	v_lshlrev_b32_e32 v99, 16, v4
	v_and_b32_e32 v101, 0xffff0000, v4
	s_waitcnt vmcnt(22)
	v_mov_b32_e32 v106, v35
	s_waitcnt vmcnt(21)
	v_mov_b32_e32 v104, v39
	v_lshlrev_b32_e32 v97, 16, v3
	v_and_b32_e32 v3, 0xffff0000, v3
	v_lshlrev_b32_e32 v103, 16, v5
	v_and_b32_e32 v5, 0xffff0000, v5
	s_waitcnt vmcnt(20)
	v_and_b32_e32 v2, 0xffff0000, v40
	v_lshlrev_b32_e32 v4, 16, v41
	v_lshlrev_b32_e32 v94, 16, v40
	s_waitcnt vmcnt(19)
	v_and_b32_e32 v100, 0xffff0000, v44
	v_lshlrev_b32_e32 v92, 16, v42
	v_and_b32_e32 v41, 0xffff0000, v41
	v_and_b32_e32 v96, 0xffff0000, v42
	v_lshlrev_b32_e32 v98, 16, v43
	v_and_b32_e32 v43, 0xffff0000, v43
	v_lshlrev_b32_e32 v102, 16, v45
	v_cndmask_b32_e64 v2, v2, 0, s[0:1]
	v_cndmask_b32_e64 v40, v4, 0, s[0:1]
	v_lshlrev_b32_e32 v4, 16, v44
	v_cndmask_b32_e64 v42, v94, 0, s[0:1]
	v_and_b32_e32 v94, 0xffff0000, v46
	v_cndmask_b32_e64 v118, v100, 0, s[0:1]
	v_lshlrev_b32_e32 v105, 16, v46
	v_cndmask_b32_e64 v44, v41, 0, s[0:1]
	v_cndmask_b32_e64 v108, v96, 0, s[0:1]
	v_cndmask_b32_e64 v112, v43, 0, s[0:1]
	s_waitcnt vmcnt(18)
	v_and_b32_e32 v114, 0xffff0000, v49
	v_lshlrev_b32_e32 v116, 16, v49
	v_cndmask_b32_e64 v41, v102, 0, s[0:1]
	v_lshlrev_b32_e32 v120, 16, v48
	v_cndmask_b32_e64 v43, v4, 0, s[0:1]
	v_mul_f32_e32 v122, v2, v37
	v_and_b32_e32 v48, 0xffff0000, v48
	v_lshlrev_b32_e32 v124, 16, v50
	v_and_b32_e32 v50, 0xffff0000, v50
	v_lshlrev_b32_e32 v126, 16, v51
	v_and_b32_e32 v128, 0xffff0000, v51
	v_cndmask_b32_e64 v109, v94, 0, s[0:1]
	s_waitcnt vmcnt(17)
	v_lshlrev_b32_e32 v117, 16, v53
	v_lshlrev_b32_e32 v121, 16, v52
	v_and_b32_e32 v49, 0xffff0000, v52
	v_mul_f32_e32 v123, v118, v37
	v_lshlrev_b32_e32 v125, 16, v54
	v_and_b32_e32 v51, 0xffff0000, v54
	v_lshlrev_b32_e32 v127, 16, v55
	v_and_b32_e32 v45, 0xffff0000, v45
	v_lshlrev_b32_e32 v107, 16, v47
	v_and_b32_e32 v113, 0xffff0000, v47
	v_cndmask_b32_e64 v46, v92, 0, s[0:1]
	v_cndmask_b32_e64 v47, v105, 0, s[0:1]
	v_and_b32_e32 v115, 0xffff0000, v53
	v_and_b32_e32 v129, 0xffff0000, v55
	v_mov_b32_e32 v119, v48
	v_pk_mov_b32 v[52:53], v[42:43], v[120:121] op_sel:[1,0]
	v_pk_mov_b32 v[54:55], v[40:41], v[116:117] op_sel:[1,0]
	v_pk_mov_b32 v[130:131], v[108:109], v[50:51] op_sel:[1,0]
	s_waitcnt vmcnt(13)
	v_pk_mul_f32 v[120:121], v[68:69], v[120:121] op_sel_hi:[0,1]
	v_pk_fma_f32 v[48:49], v[68:69], v[48:49], v[122:123] op_sel:[1,0,0]
	v_pk_mul_f32 v[68:69], v[70:71], v[116:117] op_sel_hi:[0,1]
	v_mov_b32_e32 v70, v71
	s_waitcnt vmcnt(12)
; #define LAS __attribute__((address_space(3)))
; __device__ __forceinline__ void unpack8(const u32x4 v, float (&f)[8]) { f[0] = bflo(v.x); f[1] = bfhi(v.x); f[2] = bflo(v.y); f[3] = bfhi(v.y); f[4] = bflo(v.z); f[5] = bfhi(v.z); f[6] = bflo(v.w); f[7] = bfhi(v.w); }
; __device__ __forceinline__ u32x4 pack8(const float (&f)[8]) { u32x4 o; o.x = cvtpk(f[0], f[1]); o.y = cvtpk(f[2], f[3]); o.z = cvtpk(f[4], f[5]); o.w = cvtpk(f[6], f[7]); return o; }
; __device__ __forceinline__ void p3_rows2(int row0, const bf16* PROJ, const float* sc_w, const float* sc_nw, const float* ssd_nw, const float* SSQ, bf16* Y, LAS unsigned char* scr, int lane) {
;     ...
;         for (int j = 0; j < 8; ++j) { um2[j] = halo ? um2[j] : 0.f; um1[j] = halo ? um1[j] : 0.f; }
;         unpack8(b0v, b0); unpack8(b1v, b1);
;         float y0[8], y1[8];
; #pragma unroll
;         for (int j = 0; j < 8; ++j) { y0[j] = b0[j] * (w2[j] * u0[j] + w0[j] * um2[j] + w1[j] * um1[j]); y1[j] = b1[j] * (w2[j] * u1[j] + w0[j] * um1[j] + w1[j] * u0[j]); ss0 += y0[j] * y0[j]; ss1 += y1[j] * y1[j]; }
;         *(LAS u32x4*)(scr + c0 * 2) = pack8(y0); *(LAS u32x4*)(scr + 8192 + c0 * 2) = pack8(y1);
	v_pk_mul_f32 v[116:117], v[72:73], v[124:125] op_sel_hi:[0,1]
	v_pk_mul_f32 v[50:51], v[72:73], v[50:51] op_sel:[1,0]
	v_pk_mul_f32 v[72:73], v[74:75], v[126:127] op_sel_hi:[0,1]
	v_mov_b32_e32 v74, v75
	v_cndmask_b32_e64 v110, v98, 0, s[0:1]
	v_cndmask_b32_e64 v45, v45, 0, s[0:1]
	v_cndmask_b32_e64 v111, v107, 0, s[0:1]
	v_cndmask_b32_e64 v113, v113, 0, s[0:1]
	v_lshlrev_b32_e32 v98, 16, v58
	v_and_b32_e32 v100, 0xffff0000, v58
	v_lshlrev_b32_e32 v102, 16, v59
	v_and_b32_e32 v4, 0xffff0000, v59
	v_pk_mov_b32 v[58:59], v[46:47], v[124:125] op_sel:[1,0]
	v_pk_fma_f32 v[36:37], v[42:43], v[36:37], v[120:121] op_sel_hi:[1,0,1]
	v_pk_fma_f32 v[42:43], v[118:119], v[60:61], v[48:49] op_sel:[0,1,0]
	v_pk_fma_f32 v[38:39], v[40:41], v[38:39], v[68:69] op_sel_hi:[1,0,1]
	v_pk_mul_f32 v[40:41], v[70:71], v[114:115] op_sel_hi:[0,1]
	v_pk_fma_f32 v[46:47], v[46:47], v[32:33], v[116:117] op_sel_hi:[1,0,1]
	v_pk_fma_f32 v[32:33], v[108:109], v[32:33], v[50:51] op_sel:[0,1,0]
	v_pk_mul_f32 v[48:49], v[74:75], v[128:129] op_sel_hi:[0,1]
	v_lshlrev_b32_e32 v92, 16, v56
	v_and_b32_e32 v94, 0xffff0000, v56
	v_lshlrev_b32_e32 v96, 16, v57
	v_and_b32_e32 v2, 0xffff0000, v57
	v_pk_mov_b32 v[56:57], v[44:45], v[114:115] op_sel:[1,0]
	v_pk_mov_b32 v[132:133], v[110:111], v[126:127] op_sel:[1,0]
	v_pk_mov_b32 v[134:135], v[112:113], v[128:129] op_sel:[1,0]
	v_mov_b32_e32 v136, v63
	v_mov_b32_e32 v138, v67
	v_pk_fma_f32 v[34:35], v[110:111], v[34:35], v[72:73] op_sel_hi:[1,0,1]
	v_pk_fma_f32 v[36:37], v[60:61], v[52:53], v[36:37] op_sel_hi:[0,1,1]
	v_pk_fma_f32 v[38:39], v[54:55], v[62:63], v[38:39] op_sel_hi:[1,0,1]
	v_pk_fma_f32 v[40:41], v[44:45], v[104:105], v[40:41] op_sel_hi:[1,0,1]
	v_pk_fma_f32 v[44:45], v[58:59], v[64:65], v[46:47] op_sel_hi:[1,0,1]
	v_pk_fma_f32 v[32:33], v[130:131], v[64:65], v[32:33] op_sel:[0,1,0]
	v_pk_fma_f32 v[46:47], v[112:113], v[106:107], v[48:49] op_sel_hi:[1,0,1]
	v_pk_fma_f32 v[34:35], v[132:133], v[66:67], v[34:35] op_sel_hi:[1,0,1]
	v_pk_mul_f32 v[36:37], v[36:37], v[92:93]
	v_pk_mul_f32 v[92:93], v[38:39], v[96:97]
	v_pk_fma_f32 v[38:39], v[56:57], v[136:137], v[40:41] op_sel_hi:[1,0,1]
	v_pk_mul_f32 v[96:97], v[32:33], v[100:101]
	v_pk_fma_f32 v[32:33], v[134:135], v[138:139], v[46:47] op_sel_hi:[1,0,1]
	v_pk_mul_f32 v[42:43], v[42:43], v[94:95]
	v_pk_mul_f32 v[94:95], v[44:45], v[98:99]
	v_pk_mul_f32 v[98:99], v[34:35], v[102:103]
	v_pk_fma_f32 v[8:9], v[36:37], v[36:37], v[8:9]
	v_pk_mul_f32 v[100:101], v[38:39], v[2:3]
	v_pk_mul_f32 v[102:103], v[32:33], v[4:5]
	v_cvt_pk_bf16_f32 v2, v36, v42
	v_cvt_pk_bf16_f32 v3, v92, v100
	v_cvt_pk_bf16_f32 v4, v94, v96
	v_pk_fma_f32 v[8:9], v[42:43], v[42:43], v[8:9]
	v_cvt_pk_bf16_f32 v5, v98, v102
	ds_write_b128 v31, v[2:5]
	v_cvt_pk_bf16_f32 v2, v37, v43
	v_cvt_pk_bf16_f32 v3, v93, v101
	v_cvt_pk_bf16_f32 v4, v95, v97
	v_cvt_pk_bf16_f32 v5, v99, v103
	v_pk_fma_f32 v[8:9], v[92:93], v[92:93], v[8:9]
	ds_write_b128 v31, v[2:5] offset:8192
	v_pk_fma_f32 v[8:9], v[100:101], v[100:101], v[8:9]
	v_lshl_add_u64 v[6:7], v[6:7], 0, s[28:29]
	v_pk_fma_f32 v[2:3], v[94:95], v[94:95], v[8:9]
	s_waitcnt vmcnt(11)
	v_and_b32_e32 v83, 0xffff0000, v184
	v_pk_fma_f32 v[2:3], v[96:97], v[96:97], v[2:3]
	s_waitcnt vmcnt(10)
	v_and_b32_e32 v89, 0xffff0000, v188
	v_pk_fma_f32 v[2:3], v[98:99], v[98:99], v[2:3]
	s_waitcnt vmcnt(8)
	v_lshlrev_b32_e32 v79, 16, v196
	v_lshlrev_b32_e32 v78, 16, v192
	v_lshlrev_b32_e32 v96, 16, v184
	v_lshlrev_b32_e32 v97, 16, v188
	v_pk_fma_f32 v[2:3], v[102:103], v[102:103], v[2:3]
	v_lshlrev_b32_e32 v102, 16, v190
	v_and_b32_e32 v104, 0xffff0000, v190
	v_and_b32_e32 v106, 0xffff0000, v186
	v_lshlrev_b32_e32 v108, 16, v187
	v_lshlrev_b32_e32 v107, 16, v191
	v_and_b32_e32 v109, 0xffff0000, v191
	v_lshlrev_b32_e32 v191, 16, v199
	v_lshlrev_b32_e32 v190, 16, v195
	v_cndmask_b32_e64 v83, v83, 0, s[0:1]
	v_cndmask_b32_e64 v92, v89, 0, s[0:1]
	v_cndmask_b32_e64 v97, v97, 0, s[0:1]
	v_cndmask_b32_e64 v96, v96, 0, s[0:1]
	s_waitcnt vmcnt(5)
	v_pk_mul_f32 v[98:99], v[208:209], v[78:79] op_sel_hi:[0,1]
	v_lshlrev_b32_e32 v85, 16, v185
	v_lshlrev_b32_e32 v91, 16, v189
	v_and_b32_e32 v93, 0xffff0000, v189
	v_and_b32_e32 v100, 0xffff0000, v185
	v_lshlrev_b32_e32 v9, 16, v197
	v_lshlrev_b32_e32 v8, 16, v193
	v_and_b32_e32 v185, 0xffff0000, v196
	v_and_b32_e32 v184, 0xffff0000, v192
	s_waitcnt vmcnt(2)
	v_mov_b32_e32 v86, v223
	v_cndmask_b32_e64 v105, v104, 0, s[0:1]
	v_cndmask_b32_e64 v104, v106, 0, s[0:1]
	v_cndmask_b32_e64 v107, v107, 0, s[0:1]
	v_cndmask_b32_e64 v106, v108, 0, s[0:1]
	v_pk_mul_f32 v[222:223], v[222:223], v[190:191] op_sel_hi:[0,1]
	v_pk_fma_f32 v[98:99], v[96:97], v[212:213], v[98:99] op_sel_hi:[1,0,1]
	v_pk_mov_b32 v[78:79], v[96:97], v[78:79] op_sel:[1,0]
	v_mul_f32_e32 v212, v83, v213
	v_mul_f32_e32 v213, v92, v213
	v_lshlrev_b32_e32 v87, 16, v186
	v_and_b32_e32 v4, 0xffff0000, v193
	v_and_b32_e32 v5, 0xffff0000, v197
	v_lshlrev_b32_e32 v76, 16, v200
	v_lshlrev_b32_e32 v77, 16, v204
	v_lshlrev_b32_e32 v186, 16, v194
	v_and_b32_e32 v188, 0xffff0000, v194
	v_and_b32_e32 v192, 0xffff0000, v195
	v_and_b32_e32 v195, 0xffff0000, v204
	v_and_b32_e32 v194, 0xffff0000, v200
	v_lshlrev_b32_e32 v200, 16, v202
	v_and_b32_e32 v204, 0xffff0000, v202
	v_mov_b32_e32 v202, v211
	s_waitcnt vmcnt(1)
; #define LAS __attribute__((address_space(3)))
; __device__ __forceinline__ void unpack8(const u32x4 v, float (&f)[8]) { f[0] = bflo(v.x); f[1] = bfhi(v.x); f[2] = bflo(v.y); f[3] = bfhi(v.y); f[4] = bflo(v.z); f[5] = bfhi(v.z); f[6] = bflo(v.w); f[7] = bfhi(v.w); }
; __device__ __forceinline__ u32x4 pack8(const float (&f)[8]) { u32x4 o; o.x = cvtpk(f[0], f[1]); o.y = cvtpk(f[2], f[3]); o.z = cvtpk(f[4], f[5]); o.w = cvtpk(f[6], f[7]); return o; }
; __device__ __forceinline__ void p3_rows2(int row0, const bf16* PROJ, const float* sc_w, const float* sc_nw, const float* ssd_nw, const float* SSQ, bf16* Y, LAS unsigned char* scr, int lane) {
;     ...
;         for (int j = 0; j < 8; ++j) { um2[j] = halo ? um2[j] : 0.f; um1[j] = halo ? um1[j] : 0.f; }
;         unpack8(b0v, b0); unpack8(b1v, b1);
;         float y0[8], y1[8];
; #pragma unroll
;         for (int j = 0; j < 8; ++j) { y0[j] = b0[j] * (w2[j] * u0[j] + w0[j] * um2[j] + w1[j] * um1[j]); y1[j] = b1[j] * (w2[j] * u1[j] + w0[j] * um1[j] + w1[j] * u0[j]); ss0 += y0[j] * y0[j]; ss1 += y1[j] * y1[j]; }
;         *(LAS u32x4*)(scr + c0 * 2) = pack8(y0); *(LAS u32x4*)(scr + 8192 + c0 * 2) = pack8(y1);
;     }
	v_mov_b32_e32 v88, v143
	v_cndmask_b32_e64 v94, v85, 0, s[0:1]
	v_cndmask_b32_e64 v95, v91, 0, s[0:1]
	v_cndmask_b32_e64 v101, v93, 0, s[0:1]
	v_mov_b32_e32 v93, v184
	v_pk_mul_f32 v[210:211], v[210:211], v[8:9] op_sel_hi:[0,1]
	v_pk_fma_f32 v[142:143], v[106:107], v[142:143], v[222:223] op_sel_hi:[1,0,1]
	v_pk_mov_b32 v[190:191], v[106:107], v[190:191] op_sel:[1,0]
	v_pk_fma_f32 v[222:223], v[216:217], v[78:79], v[98:99] op_sel_hi:[0,1,1]
	v_pk_fma_f32 v[184:185], v[208:209], v[184:185], v[212:213] op_sel:[1,0,0]
	v_and_b32_e32 v110, 0xffff0000, v187
	v_lshlrev_b32_e32 v187, 16, v198
	v_and_b32_e32 v189, 0xffff0000, v198
	v_and_b32_e32 v193, 0xffff0000, v199
	v_lshlrev_b32_e32 v196, 16, v201
	v_lshlrev_b32_e32 v197, 16, v205
	v_and_b32_e32 v199, 0xffff0000, v205
	v_and_b32_e32 v198, 0xffff0000, v201
	v_lshlrev_b32_e32 v201, 16, v206
	v_and_b32_e32 v205, 0xffff0000, v206
	v_lshlrev_b32_e32 v80, 16, v203
	v_and_b32_e32 v206, 0xffff0000, v203
	v_mov_b32_e32 v82, v215
	v_cndmask_b32_e64 v100, v100, 0, s[0:1]
	v_pk_mul_f32 v[202:203], v[202:203], v[4:5] op_sel_hi:[0,1]
	v_pk_fma_f32 v[210:211], v[94:95], v[214:215], v[210:211] op_sel_hi:[1,0,1]
	v_pk_mov_b32 v[8:9], v[94:95], v[8:9] op_sel:[1,0]
	s_waitcnt vmcnt(0)
	v_pk_fma_f32 v[142:143], v[190:191], v[226:227], v[142:143] op_sel_hi:[1,0,1]
	v_pk_mul_f32 v[190:191], v[222:223], v[76:77]
	v_pk_fma_f32 v[184:185], v[92:93], v[216:217], v[184:185] op_sel:[0,1,0]
	v_mov_b32_e32 v84, v219
	v_cndmask_b32_e64 v103, v102, 0, s[0:1]
	v_cndmask_b32_e64 v102, v87, 0, s[0:1]
	v_cndmask_b32_e64 v109, v109, 0, s[0:1]
	v_cndmask_b32_e64 v108, v110, 0, s[0:1]
	v_pk_mul_f32 v[110:111], v[220:221], v[186:187] op_sel_hi:[0,1]
	v_pk_mul_f32 v[220:221], v[220:221], v[188:189] op_sel:[1,0]
	v_pk_mul_f32 v[86:87], v[86:87], v[192:193] op_sel_hi:[0,1]
	v_pk_fma_f32 v[202:203], v[100:101], v[82:83], v[202:203] op_sel_hi:[1,0,1]
	v_pk_mov_b32 v[4:5], v[100:101], v[4:5] op_sel:[1,0]
	v_pk_fma_f32 v[8:9], v[8:9], v[218:219], v[210:211] op_sel_hi:[1,0,1]
	v_pk_fma_f32 v[2:3], v[190:191], v[190:191], v[2:3]
	v_pk_mul_f32 v[184:185], v[184:185], v[194:195]
	v_mov_b32_e32 v90, v227
	v_pk_fma_f32 v[214:215], v[102:103], v[140:141], v[110:111] op_sel_hi:[1,0,1]
	v_pk_mov_b32 v[186:187], v[102:103], v[186:187] op_sel:[1,0]
	v_pk_fma_f32 v[140:141], v[104:105], v[140:141], v[220:221] op_sel:[0,1,0]
	v_pk_mov_b32 v[188:189], v[104:105], v[188:189] op_sel:[1,0]
	v_pk_fma_f32 v[220:221], v[108:109], v[88:89], v[86:87] op_sel_hi:[1,0,1]
	v_pk_mov_b32 v[192:193], v[108:109], v[192:193] op_sel:[1,0]
	v_pk_fma_f32 v[4:5], v[4:5], v[84:85], v[202:203] op_sel_hi:[1,0,1]
	v_pk_mul_f32 v[8:9], v[8:9], v[196:197]
	v_pk_fma_f32 v[194:195], v[184:185], v[184:185], v[2:3]
	v_lshlrev_b32_e32 v81, 16, v207
	v_and_b32_e32 v207, 0xffff0000, v207
	v_pk_fma_f32 v[186:187], v[186:187], v[224:225], v[214:215] op_sel_hi:[1,0,1]
	v_pk_fma_f32 v[140:141], v[188:189], v[224:225], v[140:141] op_sel:[0,1,0]
	v_pk_fma_f32 v[188:189], v[192:193], v[90:91], v[220:221] op_sel_hi:[1,0,1]
	v_pk_mul_f32 v[192:193], v[4:5], v[198:199]
	v_cvt_pk_bf16_f32 v2, v190, v184
	v_pk_fma_f32 v[194:195], v[8:9], v[8:9], v[194:195]
	v_cvt_pk_bf16_f32 v3, v8, v192
	v_pk_mul_f32 v[186:187], v[186:187], v[200:201]
	v_pk_mul_f32 v[140:141], v[140:141], v[204:205]
	v_pk_mul_f32 v[142:143], v[142:143], v[80:81]
	v_pk_mul_f32 v[188:189], v[188:189], v[206:207]
	v_cvt_pk_bf16_f32 v4, v186, v140
	s_nop 0
	v_cvt_pk_bf16_f32 v5, v142, v188
	ds_write_b128 v31, v[2:5] offset:1024
	v_cvt_pk_bf16_f32 v2, v191, v185
	v_cvt_pk_bf16_f32 v3, v9, v193
	v_pk_fma_f32 v[8:9], v[192:193], v[192:193], v[194:195]
	v_cvt_pk_bf16_f32 v4, v187, v141
	v_cvt_pk_bf16_f32 v5, v143, v189
	ds_write_b128 v31, v[2:5] offset:9216
	v_pk_fma_f32 v[2:3], v[186:187], v[186:187], v[8:9]
	v_add_u32_e32 v31, 0x800, v31
	v_pk_fma_f32 v[2:3], v[140:141], v[140:141], v[2:3]
	s_nop 0
	v_pk_fma_f32 v[2:3], v[142:143], v[142:143], v[2:3]
	s_nop 0
	v_pk_fma_f32 v[8:9], v[188:189], v[188:189], v[2:3]
	s_cbranch_scc0 .LBB0_485
; __device__ __forceinline__ void p3_rows2(int row0, const bf16* PROJ, const float* sc_w, const float* sc_nw, const float* ssd_nw, const float* SSQ, bf16* Y, LAS unsigned char* scr, int lane) {
;     ...
;     const float rs0 = 1.0f / sqrtf(wave_sum(ss0) * (1.f / D_CONV) + EPS), rs1 = 1.0f / sqrtf(wave_sum(ss1) * (1.f / D_CONV) + EPS);
;     bf16* yrow = Y + (size_t)row0 * D_MIX + lane * 8;
	v_and_b32_e32 v4, 64, v30
	v_add_u32_e32 v2, 64, v4
	v_xor_b32_e32 v3, 1, v30
	v_cmp_lt_i32_e32 vcc, v3, v2
	v_xor_b32_e32 v6, 2, v30
	v_xor_b32_e32 v24, 8, v30
	v_cndmask_b32_e32 v3, v30, v3, vcc
	v_lshlrev_b32_e32 v5, 2, v3
	ds_bpermute_b32 v3, v5, v8
	v_cmp_lt_i32_e32 vcc, v6, v2
	v_xor_b32_e32 v25, 16, v30
	v_xor_b32_e32 v26, 32, v30
	v_cndmask_b32_e32 v6, v30, v6, vcc
	s_waitcnt lgkmcnt(0)
	v_add_f32_e32 v3, v8, v3
	v_lshlrev_b32_e32 v6, 2, v6
	ds_bpermute_b32 v7, v6, v3
	v_xor_b32_e32 v8, 4, v30
	v_cmp_lt_i32_e32 vcc, v8, v2
	s_waitcnt lgkmcnt(0)
	v_add_f32_e32 v3, v3, v7
	v_cndmask_b32_e32 v7, v30, v8, vcc
	v_lshlrev_b32_e32 v7, 2, v7
	ds_bpermute_b32 v8, v7, v3
	v_cmp_lt_i32_e32 vcc, v24, v2
	s_waitcnt lgkmcnt(0)
	v_add_f32_e32 v3, v3, v8
	v_cndmask_b32_e32 v8, v30, v24, vcc
	v_lshlrev_b32_e32 v8, 2, v8
	ds_bpermute_b32 v24, v8, v3
	v_cmp_lt_i32_e32 vcc, v25, v2
	s_waitcnt lgkmcnt(0)
	v_add_f32_e32 v3, v3, v24
	v_cndmask_b32_e32 v24, v30, v25, vcc
	v_cmp_lt_i32_e32 vcc, v26, v2
	v_lshlrev_b32_e32 v24, 2, v24
	ds_bpermute_b32 v25, v24, v3
	v_cndmask_b32_e32 v2, v30, v26, vcc
	ds_bpermute_b32 v26, v5, v9
	v_lshlrev_b32_e32 v2, 2, v2
	s_waitcnt lgkmcnt(1)
	v_add_f32_e32 v3, v3, v25
	ds_bpermute_b32 v25, v2, v3
	s_waitcnt lgkmcnt(1)
	v_add_f32_e32 v9, v9, v26
	ds_bpermute_b32 v26, v6, v9
	s_waitcnt lgkmcnt(1)
	v_add_f32_e32 v3, v3, v25
	v_fmamk_f32 v3, v3, 0x39800000, v28
	s_waitcnt lgkmcnt(0)
	v_add_f32_e32 v9, v9, v26
	ds_bpermute_b32 v26, v7, v9
	v_mul_f32_e32 v25, 0x4f800000, v3
	v_cmp_gt_f32_e32 vcc, s36, v3
	s_waitcnt lgkmcnt(0)
	v_add_f32_e32 v9, v9, v26
	ds_bpermute_b32 v8, v8, v9
	v_cndmask_b32_e32 v3, v3, v25, vcc
	v_sqrt_f32_e32 v25, v3
	s_waitcnt lgkmcnt(0)
	v_add_f32_e32 v8, v9, v8
	v_add_u32_e32 v27, -1, v25
	ds_bpermute_b32 v9, v24, v8
	v_fma_f32 v31, -v27, v25, v3
	v_cmp_ge_f32_e64 s[0:1], 0, v31
	v_add_u32_e32 v31, 1, v25
	s_waitcnt lgkmcnt(0)
	v_add_f32_e32 v8, v8, v9
	v_cndmask_b32_e64 v27, v25, v27, s[0:1]
	v_fma_f32 v25, -v31, v25, v3
	v_cmp_lt_f32_e64 s[0:1], 0, v25
	ds_bpermute_b32 v2, v2, v8
	s_waitcnt lgkmcnt(0)
	v_add_f32_e32 v2, v8, v2
	v_cndmask_b32_e64 v25, v27, v31, s[0:1]
	v_mul_f32_e32 v27, 0x37800000, v25
	v_cndmask_b32_e32 v25, v25, v27, vcc
	v_cmp_class_f32_e32 vcc, v3, v29
	v_fmamk_f32 v2, v2, 0x39800000, v28
	v_mul_f32_e32 v8, 0x4f800000, v2
	v_cndmask_b32_e32 v3, v25, v3, vcc
	v_div_scale_f32 v26, s[0:1], v3, v3, 1.0
	v_rcp_f32_e32 v27, v26
	s_lshl_b64 s[0:1], s[16:17], 14
	v_lshl_add_u64 v[24:25], v[16:17], 0, s[0:1]
	v_cmp_gt_f32_e64 s[0:1], s36, v2
	v_fma_f32 v31, -v26, v27, 1.0
	v_fmac_f32_e32 v27, v31, v27
	v_cndmask_b32_e64 v2, v2, v8, s[0:1]
	v_div_scale_f32 v9, vcc, 1.0, v3, 1.0
	v_sqrt_f32_e32 v8, v2
	v_mul_f32_e32 v31, v9, v27
	v_fma_f32 v32, -v26, v31, v9
	v_fmac_f32_e32 v31, v32, v27
	v_fma_f32 v9, -v26, v31, v9
	v_add_u32_e32 v26, -1, v8
	v_fma_f32 v32, -v26, v8, v2
	v_cmp_ge_f32_e64 s[4:5], 0, v32
	v_add_u32_e32 v32, 1, v8
	s_nop 0
	v_cndmask_b32_e64 v26, v8, v26, s[4:5]
	v_fma_f32 v8, -v32, v8, v2
	v_cmp_lt_f32_e64 s[4:5], 0, v8
	s_nop 1
	v_cndmask_b32_e64 v8, v26, v32, s[4:5]
	v_mul_f32_e32 v26, 0x37800000, v8
	v_cndmask_b32_e64 v8, v8, v26, s[0:1]
	v_cmp_class_f32_e64 s[0:1], v2, v29
	s_nop 1
	v_cndmask_b32_e64 v2, v8, v2, s[0:1]
	v_div_scale_f32 v26, s[0:1], v2, v2, 1.0
	v_rcp_f32_e32 v32, v26
	v_div_fmas_f32 v8, v9, v27, v31
	v_div_fixup_f32 v8, v8, v3, 1.0
	s_mov_b64 s[0:1], 0
	v_fma_f32 v3, -v26, v32, 1.0
	v_fmac_f32_e32 v32, v3, v32
	v_div_scale_f32 v3, vcc, 1.0, v2, 1.0
	v_mul_f32_e32 v9, v3, v32
	v_fma_f32 v27, -v26, v9, v3
	v_fmac_f32_e32 v9, v27, v32
	v_fma_f32 v3, -v26, v9, v3
	v_div_fmas_f32 v3, v3, v32, v9
	v_div_fixup_f32 v9, v3, v2, 1.0
	v_mov_b64_e32 v[2:3], v[20:21]
	v_mov_b32_e32 v26, v1
